# out-projection epilogue: residual-tile loads kept 6 deep in flight (SGPR-base addressing into VGPRs 232..255) instead of one load per wait; rest as previous version
# speedup vs baseline: 1.0054x; 1.0017x over previous
; #define PG8_LAS __attribute__((address_space(3)))
; __device__ __forceinline__ u32x4 pack8(const f32x4 a, const f32x4 b) { u32x4 w; w.x = pg8::cvt_pk_bf16(a[0], a[1]); w.y = pg8::cvt_pk_bf16(a[2], a[3]); w.z = pg8::cvt_pk_bf16(b[0], b[1]); w.w = pg8::cvt_pk_bf16(b[2], b[3]); return w; }
;     __device__ __forceinline__ void operator()(const f32x4 (&acc)[2][2][4][2], const pg8::Unit& u, int wr, int wc, int fr_in, int fq_in) const {
;     ...
;         const int row0 = u.pm * 256 + wr * 64 + fr, col0 = u.pn * 256 + wc * 32 + 8 * fq;
;         const bool lat = u.pm < 256; const int b = lat ? (u.pm >> 4) : 16;
;         const PG8_LAS float* gp = (const PG8_LAS float*)(lds + LDS_EPI) + wc * 32 + 8 * fq; (void)b;
;         f32x4 gv[2][2];
; #pragma unroll
;         for (int bj = 0; bj < 2; ++bj)
; #pragma unroll
;             for (int n = 0; n < 2; ++n) gv[bj][n] = *(const PG8_LAS f32x4*)(gp + bj * 128 + n * 4);
; #pragma unroll
;         for (int ai = 0; ai < 2; ++ai)
; #pragma unroll
;             for (int m = 0; m < 4; ++m) {
;                 const int row = row0 + ai * 128 + m * 16;
;                 const bf16* bp = xb + (size_t)row * DM + col0;
; #pragma unroll
;                 for (int bj = 0; bj < 2; ++bj) {
;                     const u32x4 bb = *(const u32x4*)(bp + bj * 128);
;                     const f32x4 b0 = (f32x4){bflo(bb.x), bfhi(bb.x), bflo(bb.y), bfhi(bb.y)}, b1 = (f32x4){bflo(bb.z), bfhi(bb.z), bflo(bb.w), bfhi(bb.w)};
;                     *(u32x4*)(out + (size_t)row * DM + col0 + bj * 128) = pack8(b0 + gv[bj][0] * acc[ai][bj][m][0], b1 + gv[bj][1] * acc[ai][bj][m][1]);
;                 }
.LBB0_597:
	s_lshl_b32 s47, s52, 8
	v_mov_b32_e32 v126, v168
	v_mov_b32_e32 v123, v1
	s_add_i32 s47, s47, s76
	s_or_b32 s52, s54, s77
	v_add_u32_e32 v124, s47, v123
	v_lshl_add_u32 v122, v126, 3, s52
	v_ashrrev_i32_e32 v125, 31, v124
	v_ashrrev_i32_e32 v123, 31, v122
	v_lshlrev_b64 v[166:167], 11, v[124:125]
	v_lshl_add_u64 v[124:125], s[16:17], 0, v[166:167]
	v_lshlrev_b64 v[164:165], 1, v[122:123]
	v_lshl_add_u64 v[176:177], v[124:125], 0, v[164:165]
	v_add_u32_e32 v228, v166, v164
	s_mov_b32 s98, s16
	s_mov_b32 s99, s17
	global_load_dwordx4 v[232:235], v228, s[98:99]
	s_mov_b32 s98, s16
	s_mov_b32 s99, s17
	global_load_dwordx4 v[236:239], v228, s[98:99] offset:256
	s_add_u32 s98, s16, 0x8000
	s_addc_u32 s99, s17, 0
	global_load_dwordx4 v[240:243], v228, s[98:99]
	s_add_u32 s98, s16, 0x8000
	s_addc_u32 s99, s17, 0
	global_load_dwordx4 v[244:247], v228, s[98:99] offset:256
	s_add_u32 s98, s16, 0x10000
	s_addc_u32 s99, s17, 0
	global_load_dwordx4 v[248:251], v228, s[98:99]
	s_add_u32 s98, s16, 0x10000
	s_addc_u32 s99, s17, 0
	global_load_dwordx4 v[252:255], v228, s[98:99] offset:256
	v_lshl_add_u32 v122, v126, 5, s81
	ds_read_b128 v[134:137], v122
	ds_read_b128 v[130:133], v122 offset:16
	ds_read_b128 v[126:129], v122 offset:512
	ds_read_b128 v[122:125], v122 offset:528
	s_andn2_b64 vcc, exec, s[6:7]
	s_mov_b64 s[6:7], -1
	s_waitcnt vmcnt(5)
	v_lshlrev_b32_e32 v178, 16, v232
	v_and_b32_e32 v179, 0xffff0000, v232
	v_lshlrev_b32_e32 v172, 16, v233
	v_and_b32_e32 v173, 0xffff0000, v233
	v_lshlrev_b32_e32 v180, 16, v234
	v_and_b32_e32 v181, 0xffff0000, v234
	v_lshlrev_b32_e32 v174, 16, v235
	v_and_b32_e32 v175, 0xffff0000, v235
	s_add_u32 s98, s16, 0x18000
	s_addc_u32 s99, s17, 0
	global_load_dwordx4 v[232:235], v228, s[98:99]
	s_waitcnt lgkmcnt(3)
	v_pk_fma_f32 v[144:145], v[144:145], v[136:137], v[172:173]
	v_pk_fma_f32 v[142:143], v[142:143], v[134:135], v[178:179]
	s_waitcnt lgkmcnt(2)
	v_pk_fma_f32 v[172:173], v[140:141], v[132:133], v[174:175]
	v_pk_fma_f32 v[140:141], v[138:139], v[130:131], v[180:181]
	v_cvt_pk_bf16_f32 v138, v142, v143
	v_cvt_pk_bf16_f32 v139, v144, v145
	v_lshl_add_u64 v[174:175], v[166:167], 0, s[24:25]
	v_cvt_pk_bf16_f32 v140, v140, v141
	v_cvt_pk_bf16_f32 v141, v172, v173
	v_lshl_add_u64 v[172:173], s[14:15], 0, v[166:167]
	v_lshl_add_u64 v[172:173], v[172:173], 0, v[164:165]
	v_lshl_add_u64 v[176:177], s[16:17], 0, v[174:175]
	global_store_dwordx4 v[172:173], v[138:141], off
	v_lshl_add_u64 v[176:177], v[176:177], 0, v[164:165]
	s_waitcnt vmcnt(6)
	v_lshlrev_b32_e32 v138, 16, v236
	v_and_b32_e32 v139, 0xffff0000, v236
	v_lshlrev_b32_e32 v140, 16, v237
	v_and_b32_e32 v141, 0xffff0000, v237
	v_lshlrev_b32_e32 v142, 16, v238
	v_and_b32_e32 v143, 0xffff0000, v238
	v_lshlrev_b32_e32 v144, 16, v239
	v_and_b32_e32 v145, 0xffff0000, v239
	s_add_u32 s98, s16, 0x18000
	s_addc_u32 s99, s17, 0
	global_load_dwordx4 v[236:239], v228, s[98:99] offset:256
	s_waitcnt lgkmcnt(1)
	v_pk_fma_f32 v[116:117], v[116:117], v[128:129], v[140:141]
	v_pk_fma_f32 v[114:115], v[114:115], v[126:127], v[138:139]
	s_waitcnt lgkmcnt(0)
	v_pk_fma_f32 v[138:139], v[112:113], v[124:125], v[144:145]
	v_pk_fma_f32 v[112:113], v[110:111], v[122:123], v[142:143]
	v_cvt_pk_bf16_f32 v110, v114, v115
	v_cvt_pk_bf16_f32 v111, v116, v117
	s_nop 0
	v_cvt_pk_bf16_f32 v112, v112, v113
	v_cvt_pk_bf16_f32 v113, v138, v139
	s_nop 0
	global_store_dwordx4 v[172:173], v[110:113], off offset:256
	s_waitcnt vmcnt(7)
	s_nop 0
	v_lshlrev_b32_e32 v110, 16, v240
	v_and_b32_e32 v111, 0xffff0000, v240
	v_lshlrev_b32_e32 v112, 16, v241
	v_and_b32_e32 v113, 0xffff0000, v241
	v_lshlrev_b32_e32 v114, 16, v242
	v_and_b32_e32 v115, 0xffff0000, v242
	v_lshlrev_b32_e32 v116, 16, v243
	v_and_b32_e32 v117, 0xffff0000, v243
	s_add_u32 s98, s16, 0x40000
	s_addc_u32 s99, s17, 0
	global_load_dwordx4 v[240:243], v228, s[98:99]
	v_pk_fma_f32 v[112:113], v[120:121], v[136:137], v[112:113]
	v_pk_fma_f32 v[110:111], v[118:119], v[134:135], v[110:111]
	v_pk_fma_f32 v[116:117], v[108:109], v[132:133], v[116:117]
	v_pk_fma_f32 v[108:109], v[106:107], v[130:131], v[114:115]
	v_cvt_pk_bf16_f32 v106, v110, v111
	v_cvt_pk_bf16_f32 v107, v112, v113
	v_lshl_add_u64 v[114:115], v[166:167], 0, s[26:27]
	v_cvt_pk_bf16_f32 v108, v108, v109
	v_cvt_pk_bf16_f32 v109, v116, v117
	v_lshl_add_u64 v[116:117], s[14:15], 0, v[174:175]
	v_lshl_add_u64 v[116:117], v[116:117], 0, v[164:165]
	v_lshl_add_u64 v[118:119], s[16:17], 0, v[114:115]
	global_store_dwordx4 v[116:117], v[106:109], off
	v_lshl_add_u64 v[118:119], v[118:119], 0, v[164:165]
	s_waitcnt vmcnt(8)
	v_lshlrev_b32_e32 v106, 16, v244
	v_and_b32_e32 v107, 0xffff0000, v244
	v_lshlrev_b32_e32 v108, 16, v245
	v_and_b32_e32 v109, 0xffff0000, v245
	v_lshlrev_b32_e32 v110, 16, v246
	v_and_b32_e32 v111, 0xffff0000, v246
	v_lshlrev_b32_e32 v112, 16, v247
	v_and_b32_e32 v113, 0xffff0000, v247
	s_add_u32 s98, s16, 0x40000
	s_addc_u32 s99, s17, 0
	global_load_dwordx4 v[244:247], v228, s[98:99] offset:256
	v_pk_fma_f32 v[100:101], v[100:101], v[128:129], v[108:109]
	v_pk_fma_f32 v[98:99], v[98:99], v[126:127], v[106:107]
	v_pk_fma_f32 v[106:107], v[96:97], v[124:125], v[112:113]
	v_pk_fma_f32 v[96:97], v[94:95], v[122:123], v[110:111]
	v_cvt_pk_bf16_f32 v94, v98, v99
	v_cvt_pk_bf16_f32 v95, v100, v101
	s_nop 0
	v_cvt_pk_bf16_f32 v96, v96, v97
	v_cvt_pk_bf16_f32 v97, v106, v107
	s_nop 0
	global_store_dwordx4 v[116:117], v[94:97], off offset:256
	s_waitcnt vmcnt(9)
; __device__ __forceinline__ u32x4 pack8(const f32x4 a, const f32x4 b) { u32x4 w; w.x = pg8::cvt_pk_bf16(a[0], a[1]); w.y = pg8::cvt_pk_bf16(a[2], a[3]); w.z = pg8::cvt_pk_bf16(b[0], b[1]); w.w = pg8::cvt_pk_bf16(b[2], b[3]); return w; }
;     __device__ __forceinline__ void operator()(const f32x4 (&acc)[2][2][4][2], const pg8::Unit& u, int wr, int wc, int fr_in, int fq_in) const {
;     ...
;         for (int ai = 0; ai < 2; ++ai)
; #pragma unroll
;             for (int m = 0; m < 4; ++m) {
;                 const int row = row0 + ai * 128 + m * 16;
;                 const bf16* bp = xb + (size_t)row * DM + col0;
; #pragma unroll
;                 for (int bj = 0; bj < 2; ++bj) {
;                     const u32x4 bb = *(const u32x4*)(bp + bj * 128);
;                     const f32x4 b0 = (f32x4){bflo(bb.x), bfhi(bb.x), bflo(bb.y), bfhi(bb.y)}, b1 = (f32x4){bflo(bb.z), bfhi(bb.z), bflo(bb.w), bfhi(bb.w)};
;                     *(u32x4*)(out + (size_t)row * DM + col0 + bj * 128) = pack8(b0 + gv[bj][0] * acc[ai][bj][m][0], b1 + gv[bj][1] * acc[ai][bj][m][1]);
;                 }
	s_nop 0
	v_lshlrev_b32_e32 v94, 16, v248
	v_and_b32_e32 v95, 0xffff0000, v248
	v_lshlrev_b32_e32 v96, 16, v249
	v_and_b32_e32 v97, 0xffff0000, v249
	v_lshlrev_b32_e32 v98, 16, v250
	v_and_b32_e32 v99, 0xffff0000, v250
	v_lshlrev_b32_e32 v100, 16, v251
	v_and_b32_e32 v101, 0xffff0000, v251
	s_add_u32 s98, s16, 0x48000
	s_addc_u32 s99, s17, 0
	global_load_dwordx4 v[248:251], v228, s[98:99]
	v_pk_fma_f32 v[96:97], v[104:105], v[136:137], v[96:97]
	v_pk_fma_f32 v[94:95], v[102:103], v[134:135], v[94:95]
	v_pk_fma_f32 v[100:101], v[92:93], v[132:133], v[100:101]
	v_pk_fma_f32 v[92:93], v[90:91], v[130:131], v[98:99]
	v_cvt_pk_bf16_f32 v90, v94, v95
	v_cvt_pk_bf16_f32 v91, v96, v97
	v_lshl_add_u64 v[98:99], v[166:167], 0, s[28:29]
	v_cvt_pk_bf16_f32 v92, v92, v93
	v_cvt_pk_bf16_f32 v93, v100, v101
	v_lshl_add_u64 v[100:101], s[14:15], 0, v[114:115]
	v_lshl_add_u64 v[100:101], v[100:101], 0, v[164:165]
	v_lshl_add_u64 v[102:103], s[16:17], 0, v[98:99]
	global_store_dwordx4 v[100:101], v[90:93], off
	v_lshl_add_u64 v[102:103], v[102:103], 0, v[164:165]
	s_waitcnt vmcnt(10)
	v_lshlrev_b32_e32 v90, 16, v252
	v_and_b32_e32 v91, 0xffff0000, v252
	v_lshlrev_b32_e32 v92, 16, v253
	v_and_b32_e32 v93, 0xffff0000, v253
	v_lshlrev_b32_e32 v94, 16, v254
	v_and_b32_e32 v95, 0xffff0000, v254
	v_lshlrev_b32_e32 v96, 16, v255
	v_and_b32_e32 v97, 0xffff0000, v255
	s_add_u32 s98, s16, 0x48000
	s_addc_u32 s99, s17, 0
	global_load_dwordx4 v[252:255], v228, s[98:99] offset:256
	v_pk_fma_f32 v[84:85], v[84:85], v[128:129], v[92:93]
	v_pk_fma_f32 v[82:83], v[82:83], v[126:127], v[90:91]
	v_pk_fma_f32 v[90:91], v[80:81], v[124:125], v[96:97]
	v_pk_fma_f32 v[80:81], v[78:79], v[122:123], v[94:95]
	v_cvt_pk_bf16_f32 v78, v82, v83
	v_cvt_pk_bf16_f32 v79, v84, v85
	s_nop 0
	v_cvt_pk_bf16_f32 v80, v80, v81
	v_cvt_pk_bf16_f32 v81, v90, v91
	s_nop 0
	global_store_dwordx4 v[100:101], v[78:81], off offset:256
	s_waitcnt vmcnt(11)
	s_nop 0
	v_lshlrev_b32_e32 v78, 16, v232
	v_and_b32_e32 v79, 0xffff0000, v232
	v_lshlrev_b32_e32 v80, 16, v233
	v_and_b32_e32 v81, 0xffff0000, v233
	v_lshlrev_b32_e32 v82, 16, v234
	v_and_b32_e32 v83, 0xffff0000, v234
	v_lshlrev_b32_e32 v84, 16, v235
	v_and_b32_e32 v85, 0xffff0000, v235
	s_add_u32 s98, s16, 0x50000
	s_addc_u32 s99, s17, 0
	global_load_dwordx4 v[232:235], v228, s[98:99]
	v_pk_fma_f32 v[80:81], v[88:89], v[136:137], v[80:81]
	v_pk_fma_f32 v[78:79], v[86:87], v[134:135], v[78:79]
	v_pk_fma_f32 v[84:85], v[76:77], v[132:133], v[84:85]
	v_pk_fma_f32 v[76:77], v[74:75], v[130:131], v[82:83]
	v_cvt_pk_bf16_f32 v74, v78, v79
	v_cvt_pk_bf16_f32 v75, v80, v81
	v_lshl_add_u64 v[82:83], v[166:167], 0, s[10:11]
	v_cvt_pk_bf16_f32 v76, v76, v77
	v_cvt_pk_bf16_f32 v77, v84, v85
	v_lshl_add_u64 v[84:85], s[14:15], 0, v[98:99]
	v_lshl_add_u64 v[84:85], v[84:85], 0, v[164:165]
	v_lshl_add_u64 v[86:87], s[16:17], 0, v[82:83]
	global_store_dwordx4 v[84:85], v[74:77], off
	v_lshl_add_u64 v[86:87], v[86:87], 0, v[164:165]
	s_waitcnt vmcnt(11)
	v_lshlrev_b32_e32 v74, 16, v236
	v_and_b32_e32 v75, 0xffff0000, v236
	v_lshlrev_b32_e32 v76, 16, v237
	v_and_b32_e32 v77, 0xffff0000, v237
	v_lshlrev_b32_e32 v78, 16, v238
	v_and_b32_e32 v79, 0xffff0000, v238
	v_lshlrev_b32_e32 v80, 16, v239
	v_and_b32_e32 v81, 0xffff0000, v239
	s_add_u32 s98, s16, 0x50000
	s_addc_u32 s99, s17, 0
	global_load_dwordx4 v[236:239], v228, s[98:99] offset:256
	v_pk_fma_f32 v[72:73], v[72:73], v[128:129], v[76:77]
	v_pk_fma_f32 v[70:71], v[70:71], v[126:127], v[74:75]
	v_pk_fma_f32 v[74:75], v[68:69], v[124:125], v[80:81]
	v_pk_fma_f32 v[68:69], v[66:67], v[122:123], v[78:79]
	v_cvt_pk_bf16_f32 v66, v70, v71
	v_cvt_pk_bf16_f32 v67, v72, v73
	s_nop 0
	v_cvt_pk_bf16_f32 v68, v68, v69
	v_cvt_pk_bf16_f32 v69, v74, v75
	s_nop 0
	global_store_dwordx4 v[84:85], v[66:69], off offset:256
	s_waitcnt vmcnt(11)
	s_nop 0
	v_lshlrev_b32_e32 v66, 16, v240
	v_and_b32_e32 v67, 0xffff0000, v240
	v_lshlrev_b32_e32 v68, 16, v241
	v_and_b32_e32 v69, 0xffff0000, v241
	v_lshlrev_b32_e32 v70, 16, v242
	v_and_b32_e32 v71, 0xffff0000, v242
	v_lshlrev_b32_e32 v72, 16, v243
	v_and_b32_e32 v73, 0xffff0000, v243
	s_add_u32 s98, s16, 0x58000
	s_addc_u32 s99, s17, 0
	global_load_dwordx4 v[240:243], v228, s[98:99]
	v_pk_fma_f32 v[64:65], v[64:65], v[136:137], v[68:69]
	v_pk_fma_f32 v[62:63], v[62:63], v[134:135], v[66:67]
	v_pk_fma_f32 v[66:67], v[60:61], v[132:133], v[72:73]
	v_pk_fma_f32 v[60:61], v[58:59], v[130:131], v[70:71]
	v_cvt_pk_bf16_f32 v58, v62, v63
	v_cvt_pk_bf16_f32 v59, v64, v65
	v_lshl_add_u64 v[68:69], s[14:15], 0, v[82:83]
	v_cvt_pk_bf16_f32 v60, v60, v61
	v_cvt_pk_bf16_f32 v61, v66, v67
	v_lshl_add_u64 v[66:67], v[166:167], 0, s[30:31]
	v_lshl_add_u64 v[68:69], v[68:69], 0, v[164:165]
	v_lshl_add_u64 v[70:71], s[16:17], 0, v[66:67]
	global_store_dwordx4 v[68:69], v[58:61], off
	v_lshl_add_u64 v[70:71], v[70:71], 0, v[164:165]
	s_waitcnt vmcnt(11)
	v_lshlrev_b32_e32 v58, 16, v244
	v_and_b32_e32 v59, 0xffff0000, v244
	v_lshlrev_b32_e32 v60, 16, v245
	v_and_b32_e32 v61, 0xffff0000, v245
	v_lshlrev_b32_e32 v62, 16, v246
	v_and_b32_e32 v63, 0xffff0000, v246
	v_lshlrev_b32_e32 v64, 16, v247
	v_and_b32_e32 v65, 0xffff0000, v247
	s_add_u32 s98, s16, 0x58000
	s_addc_u32 s99, s17, 0
	global_load_dwordx4 v[244:247], v228, s[98:99] offset:256
	v_pk_fma_f32 v[52:53], v[52:53], v[128:129], v[60:61]
	v_pk_fma_f32 v[50:51], v[50:51], v[126:127], v[58:59]
	v_pk_fma_f32 v[58:59], v[48:49], v[124:125], v[64:65]
	v_pk_fma_f32 v[48:49], v[46:47], v[122:123], v[62:63]
	v_cvt_pk_bf16_f32 v46, v50, v51
	v_cvt_pk_bf16_f32 v47, v52, v53
	s_nop 0
	v_cvt_pk_bf16_f32 v48, v48, v49
	v_cvt_pk_bf16_f32 v49, v58, v59
	s_nop 0
	global_store_dwordx4 v[68:69], v[46:49], off offset:256
	s_waitcnt vmcnt(11)
; __device__ __forceinline__ u32x4 pack8(const f32x4 a, const f32x4 b) { u32x4 w; w.x = pg8::cvt_pk_bf16(a[0], a[1]); w.y = pg8::cvt_pk_bf16(a[2], a[3]); w.z = pg8::cvt_pk_bf16(b[0], b[1]); w.w = pg8::cvt_pk_bf16(b[2], b[3]); return w; }
;     __device__ __forceinline__ void operator()(const f32x4 (&acc)[2][2][4][2], const pg8::Unit& u, int wr, int wc, int fr_in, int fq_in) const {
;     ...
;         for (int ai = 0; ai < 2; ++ai)
; #pragma unroll
;             for (int m = 0; m < 4; ++m) {
;                 const int row = row0 + ai * 128 + m * 16;
;                 const bf16* bp = xb + (size_t)row * DM + col0;
; #pragma unroll
;                 for (int bj = 0; bj < 2; ++bj) {
;                     const u32x4 bb = *(const u32x4*)(bp + bj * 128);
;                     const f32x4 b0 = (f32x4){bflo(bb.x), bfhi(bb.x), bflo(bb.y), bfhi(bb.y)}, b1 = (f32x4){bflo(bb.z), bfhi(bb.z), bflo(bb.w), bfhi(bb.w)};
;                     *(u32x4*)(out + (size_t)row * DM + col0 + bj * 128) = pack8(b0 + gv[bj][0] * acc[ai][bj][m][0], b1 + gv[bj][1] * acc[ai][bj][m][1]);
;                 }
	s_nop 0
	v_lshlrev_b32_e32 v46, 16, v248
	v_and_b32_e32 v47, 0xffff0000, v248
	v_lshlrev_b32_e32 v48, 16, v249
	v_and_b32_e32 v49, 0xffff0000, v249
	v_lshlrev_b32_e32 v50, 16, v250
	v_and_b32_e32 v51, 0xffff0000, v250
	v_lshlrev_b32_e32 v52, 16, v251
	v_and_b32_e32 v53, 0xffff0000, v251
	v_pk_fma_f32 v[48:49], v[56:57], v[136:137], v[48:49]
	v_pk_fma_f32 v[46:47], v[54:55], v[134:135], v[46:47]
	v_pk_fma_f32 v[52:53], v[44:45], v[132:133], v[52:53]
	v_pk_fma_f32 v[44:45], v[42:43], v[130:131], v[50:51]
	v_cvt_pk_bf16_f32 v42, v46, v47
	v_cvt_pk_bf16_f32 v43, v48, v49
	v_lshl_add_u64 v[50:51], v[166:167], 0, s[34:35]
	v_cvt_pk_bf16_f32 v44, v44, v45
	v_cvt_pk_bf16_f32 v45, v52, v53
	v_lshl_add_u64 v[52:53], s[14:15], 0, v[66:67]
	v_lshl_add_u64 v[52:53], v[52:53], 0, v[164:165]
	v_lshl_add_u64 v[54:55], s[16:17], 0, v[50:51]
	global_store_dwordx4 v[52:53], v[42:45], off
	v_lshl_add_u64 v[54:55], v[54:55], 0, v[164:165]
	s_waitcnt vmcnt(10)
	v_lshlrev_b32_e32 v42, 16, v252
	v_and_b32_e32 v43, 0xffff0000, v252
	v_lshlrev_b32_e32 v44, 16, v253
	v_and_b32_e32 v45, 0xffff0000, v253
	v_lshlrev_b32_e32 v46, 16, v254
	v_and_b32_e32 v47, 0xffff0000, v254
	v_lshlrev_b32_e32 v48, 16, v255
	v_and_b32_e32 v49, 0xffff0000, v255
	v_pk_fma_f32 v[36:37], v[36:37], v[128:129], v[44:45]
	v_pk_fma_f32 v[34:35], v[34:35], v[126:127], v[42:43]
	v_pk_fma_f32 v[42:43], v[32:33], v[124:125], v[48:49]
	v_pk_fma_f32 v[32:33], v[30:31], v[122:123], v[46:47]
	v_cvt_pk_bf16_f32 v30, v34, v35
	v_cvt_pk_bf16_f32 v31, v36, v37
	s_nop 0
	v_cvt_pk_bf16_f32 v32, v32, v33
	v_cvt_pk_bf16_f32 v33, v42, v43
	s_nop 0
	global_store_dwordx4 v[52:53], v[30:33], off offset:256
	s_waitcnt vmcnt(9)
	s_nop 0
	v_lshlrev_b32_e32 v30, 16, v232
	v_and_b32_e32 v31, 0xffff0000, v232
	v_lshlrev_b32_e32 v32, 16, v233
	v_and_b32_e32 v33, 0xffff0000, v233
	v_lshlrev_b32_e32 v34, 16, v234
	v_and_b32_e32 v35, 0xffff0000, v234
	v_lshlrev_b32_e32 v36, 16, v235
	v_and_b32_e32 v37, 0xffff0000, v235
	v_pk_fma_f32 v[32:33], v[40:41], v[136:137], v[32:33]
	v_pk_fma_f32 v[30:31], v[38:39], v[134:135], v[30:31]
	v_pk_fma_f32 v[36:37], v[28:29], v[132:133], v[36:37]
	v_pk_fma_f32 v[28:29], v[26:27], v[130:131], v[34:35]
	v_cvt_pk_bf16_f32 v26, v30, v31
	v_cvt_pk_bf16_f32 v27, v32, v33
	v_lshl_add_u64 v[34:35], v[166:167], 0, s[44:45]
	v_cvt_pk_bf16_f32 v28, v28, v29
	v_cvt_pk_bf16_f32 v29, v36, v37
	v_lshl_add_u64 v[36:37], s[14:15], 0, v[50:51]
	v_lshl_add_u64 v[36:37], v[36:37], 0, v[164:165]
	v_lshl_add_u64 v[38:39], s[16:17], 0, v[34:35]
	global_store_dwordx4 v[36:37], v[26:29], off
	v_lshl_add_u64 v[38:39], v[38:39], 0, v[164:165]
	s_waitcnt vmcnt(8)
	v_lshlrev_b32_e32 v26, 16, v236
	v_and_b32_e32 v27, 0xffff0000, v236
	v_lshlrev_b32_e32 v28, 16, v237
	v_and_b32_e32 v29, 0xffff0000, v237
	v_lshlrev_b32_e32 v30, 16, v238
	v_and_b32_e32 v31, 0xffff0000, v238
	v_lshlrev_b32_e32 v32, 16, v239
	v_and_b32_e32 v33, 0xffff0000, v239
	v_pk_fma_f32 v[20:21], v[20:21], v[128:129], v[28:29]
	v_pk_fma_f32 v[18:19], v[18:19], v[126:127], v[26:27]
	v_pk_fma_f32 v[26:27], v[16:17], v[124:125], v[32:33]
	v_pk_fma_f32 v[16:17], v[14:15], v[122:123], v[30:31]
	v_cvt_pk_bf16_f32 v14, v18, v19
	v_cvt_pk_bf16_f32 v15, v20, v21
	s_nop 0
	v_cvt_pk_bf16_f32 v16, v16, v17
	v_cvt_pk_bf16_f32 v17, v26, v27
	s_nop 0
	global_store_dwordx4 v[36:37], v[14:17], off offset:256
	s_waitcnt vmcnt(7)
	s_nop 0
	v_lshlrev_b32_e32 v14, 16, v240
	v_and_b32_e32 v15, 0xffff0000, v240
	v_lshlrev_b32_e32 v16, 16, v241
	v_and_b32_e32 v17, 0xffff0000, v241
	v_lshlrev_b32_e32 v18, 16, v242
	v_and_b32_e32 v19, 0xffff0000, v242
	v_lshlrev_b32_e32 v20, 16, v243
	v_and_b32_e32 v21, 0xffff0000, v243
	v_pk_fma_f32 v[16:17], v[24:25], v[136:137], v[16:17]
	v_pk_fma_f32 v[14:15], v[22:23], v[134:135], v[14:15]
	v_pk_fma_f32 v[20:21], v[12:13], v[132:133], v[20:21]
	v_pk_fma_f32 v[12:13], v[10:11], v[130:131], v[18:19]
	v_cvt_pk_bf16_f32 v10, v14, v15
	v_cvt_pk_bf16_f32 v11, v16, v17
	v_lshl_add_u64 v[18:19], s[14:15], 0, v[34:35]
	v_cvt_pk_bf16_f32 v12, v12, v13
	v_cvt_pk_bf16_f32 v13, v20, v21
	v_lshl_add_u64 v[18:19], v[18:19], 0, v[164:165]
	global_store_dwordx4 v[18:19], v[10:13], off
	s_waitcnt vmcnt(6)
	s_nop 0
	v_lshlrev_b32_e32 v10, 16, v244
	v_and_b32_e32 v11, 0xffff0000, v244
	v_lshlrev_b32_e32 v12, 16, v245
	v_and_b32_e32 v13, 0xffff0000, v245
	v_lshlrev_b32_e32 v14, 16, v246
	v_and_b32_e32 v15, 0xffff0000, v246
	v_lshlrev_b32_e32 v16, 16, v247
	v_and_b32_e32 v17, 0xffff0000, v247
	v_pk_fma_f32 v[6:7], v[6:7], v[126:127], v[10:11]
	v_pk_fma_f32 v[10:11], v[4:5], v[124:125], v[16:17]
	v_pk_fma_f32 v[4:5], v[2:3], v[122:123], v[14:15]
	v_pk_fma_f32 v[8:9], v[8:9], v[128:129], v[12:13]
	v_cvt_pk_bf16_f32 v2, v6, v7
	s_nop 0
	v_cvt_pk_bf16_f32 v3, v8, v9
	v_cvt_pk_bf16_f32 v4, v4, v5
	v_cvt_pk_bf16_f32 v5, v10, v11
	global_store_dwordx4 v[18:19], v[2:5], off offset:256
	s_cbranch_vccnz .LBB0_588
	s_andn2_b64 vcc, exec, s[12:13]
	s_cbranch_vccnz .LBB0_587
	s_barrier
	s_branch .LBB0_587

; #define PG8_LAS __attribute__((address_space(3)))
; __device__ __forceinline__ u32x4 pack8(const f32x4 a, const f32x4 b) { u32x4 w; w.x = pg8::cvt_pk_bf16(a[0], a[1]); w.y = pg8::cvt_pk_bf16(a[2], a[3]); w.z = pg8::cvt_pk_bf16(b[0], b[1]); w.w = pg8::cvt_pk_bf16(b[2], b[3]); return w; }
;     __device__ __forceinline__ void operator()(const f32x4 (&acc)[2][2][4][2], const pg8::Unit& u, int wr, int wc, int fr_in, int fq_in) const {
;     ...
;         const int row0 = u.pm * 256 + wr * 64 + fr, col0 = u.pn * 256 + wc * 32 + 8 * fq;
;         const bool lat = u.pm < 256; const int b = lat ? (u.pm >> 4) : 16;
;         const PG8_LAS float* gp = (const PG8_LAS float*)(lds + LDS_EPI) + wc * 32 + 8 * fq; (void)b;
;         f32x4 gv[2][2];
; #pragma unroll
;         for (int bj = 0; bj < 2; ++bj)
; #pragma unroll
;             for (int n = 0; n < 2; ++n) gv[bj][n] = *(const PG8_LAS f32x4*)(gp + bj * 128 + n * 4);
; #pragma unroll
;         for (int ai = 0; ai < 2; ++ai)
; #pragma unroll
;             for (int m = 0; m < 4; ++m) {
;                 const int row = row0 + ai * 128 + m * 16;
;                 const bf16* bp = xb + (size_t)row * DM + col0;
; #pragma unroll
;                 for (int bj = 0; bj < 2; ++bj) {
;                     const u32x4 bb = *(const u32x4*)(bp + bj * 128);
;                     const f32x4 b0 = (f32x4){bflo(bb.x), bfhi(bb.x), bflo(bb.y), bfhi(bb.y)}, b1 = (f32x4){bflo(bb.z), bfhi(bb.z), bflo(bb.w), bfhi(bb.w)};
;                     *(u32x4*)(out + (size_t)row * DM + col0 + bj * 128) = pack8(b0 + gv[bj][0] * acc[ai][bj][m][0], b1 + gv[bj][1] * acc[ai][bj][m][1]);
;                 }
.LBB0_1502:
	s_lshl_b32 s45, s50, 8
	v_mov_b32_e32 v126, v168
	v_mov_b32_e32 v123, v1
	s_add_i32 s45, s45, s73
	s_or_b32 s50, s52, s74
	v_add_u32_e32 v124, s45, v123
	v_lshl_add_u32 v122, v126, 3, s50
	v_ashrrev_i32_e32 v125, 31, v124
	v_ashrrev_i32_e32 v123, 31, v122
	v_lshlrev_b64 v[166:167], 11, v[124:125]
	v_lshl_add_u64 v[124:125], s[14:15], 0, v[166:167]
	v_lshlrev_b64 v[164:165], 1, v[122:123]
	v_lshl_add_u64 v[176:177], v[124:125], 0, v[164:165]
	v_add_u32_e32 v228, v166, v164
	s_mov_b32 s98, s14
	s_mov_b32 s99, s15
	global_load_dwordx4 v[232:235], v228, s[98:99]
	s_mov_b32 s98, s14
	s_mov_b32 s99, s15
	global_load_dwordx4 v[236:239], v228, s[98:99] offset:256
	s_add_u32 s98, s14, 0x8000
	s_addc_u32 s99, s15, 0
	global_load_dwordx4 v[240:243], v228, s[98:99]
	s_add_u32 s98, s14, 0x8000
	s_addc_u32 s99, s15, 0
	global_load_dwordx4 v[244:247], v228, s[98:99] offset:256
	s_add_u32 s98, s14, 0x10000
	s_addc_u32 s99, s15, 0
	global_load_dwordx4 v[248:251], v228, s[98:99]
	s_add_u32 s98, s14, 0x10000
	s_addc_u32 s99, s15, 0
	global_load_dwordx4 v[252:255], v228, s[98:99] offset:256
	v_lshl_add_u32 v122, v126, 5, s78
	ds_read_b128 v[134:137], v122
	ds_read_b128 v[130:133], v122 offset:16
	ds_read_b128 v[126:129], v122 offset:512
	ds_read_b128 v[122:125], v122 offset:528
	s_andn2_b64 vcc, exec, s[4:5]
	s_mov_b64 s[4:5], -1
	s_waitcnt vmcnt(5)
	v_lshlrev_b32_e32 v178, 16, v232
	v_and_b32_e32 v179, 0xffff0000, v232
	v_lshlrev_b32_e32 v172, 16, v233
	v_and_b32_e32 v173, 0xffff0000, v233
	v_lshlrev_b32_e32 v180, 16, v234
	v_and_b32_e32 v181, 0xffff0000, v234
	v_lshlrev_b32_e32 v174, 16, v235
	v_and_b32_e32 v175, 0xffff0000, v235
	s_add_u32 s98, s14, 0x18000
	s_addc_u32 s99, s15, 0
	global_load_dwordx4 v[232:235], v228, s[98:99]
	s_waitcnt lgkmcnt(3)
	v_pk_fma_f32 v[144:145], v[144:145], v[136:137], v[172:173]
	v_pk_fma_f32 v[142:143], v[142:143], v[134:135], v[178:179]
	s_waitcnt lgkmcnt(2)
	v_pk_fma_f32 v[172:173], v[140:141], v[132:133], v[174:175]
	v_pk_fma_f32 v[140:141], v[138:139], v[130:131], v[180:181]
	v_cvt_pk_bf16_f32 v138, v142, v143
	v_cvt_pk_bf16_f32 v139, v144, v145
	v_lshl_add_u64 v[174:175], v[166:167], 0, s[22:23]
	v_cvt_pk_bf16_f32 v140, v140, v141
	v_cvt_pk_bf16_f32 v141, v172, v173
	v_lshl_add_u64 v[172:173], s[12:13], 0, v[166:167]
	v_lshl_add_u64 v[172:173], v[172:173], 0, v[164:165]
	v_lshl_add_u64 v[176:177], s[14:15], 0, v[174:175]
	global_store_dwordx4 v[172:173], v[138:141], off
	v_lshl_add_u64 v[176:177], v[176:177], 0, v[164:165]
	s_waitcnt vmcnt(6)
	v_lshlrev_b32_e32 v138, 16, v236
	v_and_b32_e32 v139, 0xffff0000, v236
	v_lshlrev_b32_e32 v140, 16, v237
	v_and_b32_e32 v141, 0xffff0000, v237
	v_lshlrev_b32_e32 v142, 16, v238
	v_and_b32_e32 v143, 0xffff0000, v238
	v_lshlrev_b32_e32 v144, 16, v239
	v_and_b32_e32 v145, 0xffff0000, v239
	s_add_u32 s98, s14, 0x18000
	s_addc_u32 s99, s15, 0
	global_load_dwordx4 v[236:239], v228, s[98:99] offset:256
	s_waitcnt lgkmcnt(1)
	v_pk_fma_f32 v[116:117], v[116:117], v[128:129], v[140:141]
	v_pk_fma_f32 v[114:115], v[114:115], v[126:127], v[138:139]
	s_waitcnt lgkmcnt(0)
	v_pk_fma_f32 v[138:139], v[112:113], v[124:125], v[144:145]
	v_pk_fma_f32 v[112:113], v[110:111], v[122:123], v[142:143]
	v_cvt_pk_bf16_f32 v110, v114, v115
	v_cvt_pk_bf16_f32 v111, v116, v117
	s_nop 0
	v_cvt_pk_bf16_f32 v112, v112, v113
	v_cvt_pk_bf16_f32 v113, v138, v139
	s_nop 0
	global_store_dwordx4 v[172:173], v[110:113], off offset:256
	s_waitcnt vmcnt(7)
	s_nop 0
	v_lshlrev_b32_e32 v110, 16, v240
	v_and_b32_e32 v111, 0xffff0000, v240
	v_lshlrev_b32_e32 v112, 16, v241
	v_and_b32_e32 v113, 0xffff0000, v241
	v_lshlrev_b32_e32 v114, 16, v242
	v_and_b32_e32 v115, 0xffff0000, v242
	v_lshlrev_b32_e32 v116, 16, v243
	v_and_b32_e32 v117, 0xffff0000, v243
	s_add_u32 s98, s14, 0x40000
	s_addc_u32 s99, s15, 0
	global_load_dwordx4 v[240:243], v228, s[98:99]
	v_pk_fma_f32 v[112:113], v[120:121], v[136:137], v[112:113]
	v_pk_fma_f32 v[110:111], v[118:119], v[134:135], v[110:111]
	v_pk_fma_f32 v[116:117], v[108:109], v[132:133], v[116:117]
	v_pk_fma_f32 v[108:109], v[106:107], v[130:131], v[114:115]
	v_cvt_pk_bf16_f32 v106, v110, v111
	v_cvt_pk_bf16_f32 v107, v112, v113
	v_lshl_add_u64 v[114:115], v[166:167], 0, s[24:25]
	v_cvt_pk_bf16_f32 v108, v108, v109
	v_cvt_pk_bf16_f32 v109, v116, v117
	v_lshl_add_u64 v[116:117], s[12:13], 0, v[174:175]
	v_lshl_add_u64 v[116:117], v[116:117], 0, v[164:165]
	v_lshl_add_u64 v[118:119], s[14:15], 0, v[114:115]
	global_store_dwordx4 v[116:117], v[106:109], off
	v_lshl_add_u64 v[118:119], v[118:119], 0, v[164:165]
	s_waitcnt vmcnt(8)
	v_lshlrev_b32_e32 v106, 16, v244
	v_and_b32_e32 v107, 0xffff0000, v244
	v_lshlrev_b32_e32 v108, 16, v245
	v_and_b32_e32 v109, 0xffff0000, v245
	v_lshlrev_b32_e32 v110, 16, v246
	v_and_b32_e32 v111, 0xffff0000, v246
	v_lshlrev_b32_e32 v112, 16, v247
	v_and_b32_e32 v113, 0xffff0000, v247
	s_add_u32 s98, s14, 0x40000
	s_addc_u32 s99, s15, 0
	global_load_dwordx4 v[244:247], v228, s[98:99] offset:256
	v_pk_fma_f32 v[100:101], v[100:101], v[128:129], v[108:109]
	v_pk_fma_f32 v[98:99], v[98:99], v[126:127], v[106:107]
	v_pk_fma_f32 v[106:107], v[96:97], v[124:125], v[112:113]
	v_pk_fma_f32 v[96:97], v[94:95], v[122:123], v[110:111]
	v_cvt_pk_bf16_f32 v94, v98, v99
	v_cvt_pk_bf16_f32 v95, v100, v101
	s_nop 0
	v_cvt_pk_bf16_f32 v96, v96, v97
	v_cvt_pk_bf16_f32 v97, v106, v107
	s_nop 0
	global_store_dwordx4 v[116:117], v[94:97], off offset:256
	s_waitcnt vmcnt(9)
; __device__ __forceinline__ u32x4 pack8(const f32x4 a, const f32x4 b) { u32x4 w; w.x = pg8::cvt_pk_bf16(a[0], a[1]); w.y = pg8::cvt_pk_bf16(a[2], a[3]); w.z = pg8::cvt_pk_bf16(b[0], b[1]); w.w = pg8::cvt_pk_bf16(b[2], b[3]); return w; }
;     __device__ __forceinline__ void operator()(const f32x4 (&acc)[2][2][4][2], const pg8::Unit& u, int wr, int wc, int fr_in, int fq_in) const {
;     ...
;         for (int ai = 0; ai < 2; ++ai)
; #pragma unroll
;             for (int m = 0; m < 4; ++m) {
;                 const int row = row0 + ai * 128 + m * 16;
;                 const bf16* bp = xb + (size_t)row * DM + col0;
; #pragma unroll
;                 for (int bj = 0; bj < 2; ++bj) {
;                     const u32x4 bb = *(const u32x4*)(bp + bj * 128);
;                     const f32x4 b0 = (f32x4){bflo(bb.x), bfhi(bb.x), bflo(bb.y), bfhi(bb.y)}, b1 = (f32x4){bflo(bb.z), bfhi(bb.z), bflo(bb.w), bfhi(bb.w)};
;                     *(u32x4*)(out + (size_t)row * DM + col0 + bj * 128) = pack8(b0 + gv[bj][0] * acc[ai][bj][m][0], b1 + gv[bj][1] * acc[ai][bj][m][1]);
;                 }
	s_nop 0
	v_lshlrev_b32_e32 v94, 16, v248
	v_and_b32_e32 v95, 0xffff0000, v248
	v_lshlrev_b32_e32 v96, 16, v249
	v_and_b32_e32 v97, 0xffff0000, v249
	v_lshlrev_b32_e32 v98, 16, v250
	v_and_b32_e32 v99, 0xffff0000, v250
	v_lshlrev_b32_e32 v100, 16, v251
	v_and_b32_e32 v101, 0xffff0000, v251
	s_add_u32 s98, s14, 0x48000
	s_addc_u32 s99, s15, 0
	global_load_dwordx4 v[248:251], v228, s[98:99]
	v_pk_fma_f32 v[96:97], v[104:105], v[136:137], v[96:97]
	v_pk_fma_f32 v[94:95], v[102:103], v[134:135], v[94:95]
	v_pk_fma_f32 v[100:101], v[92:93], v[132:133], v[100:101]
	v_pk_fma_f32 v[92:93], v[90:91], v[130:131], v[98:99]
	v_cvt_pk_bf16_f32 v90, v94, v95
	v_cvt_pk_bf16_f32 v91, v96, v97
	v_lshl_add_u64 v[98:99], v[166:167], 0, s[26:27]
	v_cvt_pk_bf16_f32 v92, v92, v93
	v_cvt_pk_bf16_f32 v93, v100, v101
	v_lshl_add_u64 v[100:101], s[12:13], 0, v[114:115]
	v_lshl_add_u64 v[100:101], v[100:101], 0, v[164:165]
	v_lshl_add_u64 v[102:103], s[14:15], 0, v[98:99]
	global_store_dwordx4 v[100:101], v[90:93], off
	v_lshl_add_u64 v[102:103], v[102:103], 0, v[164:165]
	s_waitcnt vmcnt(10)
	v_lshlrev_b32_e32 v90, 16, v252
	v_and_b32_e32 v91, 0xffff0000, v252
	v_lshlrev_b32_e32 v92, 16, v253
	v_and_b32_e32 v93, 0xffff0000, v253
	v_lshlrev_b32_e32 v94, 16, v254
	v_and_b32_e32 v95, 0xffff0000, v254
	v_lshlrev_b32_e32 v96, 16, v255
	v_and_b32_e32 v97, 0xffff0000, v255
	s_add_u32 s98, s14, 0x48000
	s_addc_u32 s99, s15, 0
	global_load_dwordx4 v[252:255], v228, s[98:99] offset:256
	v_pk_fma_f32 v[84:85], v[84:85], v[128:129], v[92:93]
	v_pk_fma_f32 v[82:83], v[82:83], v[126:127], v[90:91]
	v_pk_fma_f32 v[90:91], v[80:81], v[124:125], v[96:97]
	v_pk_fma_f32 v[80:81], v[78:79], v[122:123], v[94:95]
	v_cvt_pk_bf16_f32 v78, v82, v83
	v_cvt_pk_bf16_f32 v79, v84, v85
	s_nop 0
	v_cvt_pk_bf16_f32 v80, v80, v81
	v_cvt_pk_bf16_f32 v81, v90, v91
	s_nop 0
	global_store_dwordx4 v[100:101], v[78:81], off offset:256
	s_waitcnt vmcnt(11)
	s_nop 0
	v_lshlrev_b32_e32 v78, 16, v232
	v_and_b32_e32 v79, 0xffff0000, v232
	v_lshlrev_b32_e32 v80, 16, v233
	v_and_b32_e32 v81, 0xffff0000, v233
	v_lshlrev_b32_e32 v82, 16, v234
	v_and_b32_e32 v83, 0xffff0000, v234
	v_lshlrev_b32_e32 v84, 16, v235
	v_and_b32_e32 v85, 0xffff0000, v235
	s_add_u32 s98, s14, 0x50000
	s_addc_u32 s99, s15, 0
	global_load_dwordx4 v[232:235], v228, s[98:99]
	v_pk_fma_f32 v[80:81], v[88:89], v[136:137], v[80:81]
	v_pk_fma_f32 v[78:79], v[86:87], v[134:135], v[78:79]
	v_pk_fma_f32 v[84:85], v[76:77], v[132:133], v[84:85]
	v_pk_fma_f32 v[76:77], v[74:75], v[130:131], v[82:83]
	v_cvt_pk_bf16_f32 v74, v78, v79
	v_cvt_pk_bf16_f32 v75, v80, v81
	v_lshl_add_u64 v[82:83], v[166:167], 0, s[8:9]
	v_cvt_pk_bf16_f32 v76, v76, v77
	v_cvt_pk_bf16_f32 v77, v84, v85
	v_lshl_add_u64 v[84:85], s[12:13], 0, v[98:99]
	v_lshl_add_u64 v[84:85], v[84:85], 0, v[164:165]
	v_lshl_add_u64 v[86:87], s[14:15], 0, v[82:83]
	global_store_dwordx4 v[84:85], v[74:77], off
	v_lshl_add_u64 v[86:87], v[86:87], 0, v[164:165]
	s_waitcnt vmcnt(11)
	v_lshlrev_b32_e32 v74, 16, v236
	v_and_b32_e32 v75, 0xffff0000, v236
	v_lshlrev_b32_e32 v76, 16, v237
	v_and_b32_e32 v77, 0xffff0000, v237
	v_lshlrev_b32_e32 v78, 16, v238
	v_and_b32_e32 v79, 0xffff0000, v238
	v_lshlrev_b32_e32 v80, 16, v239
	v_and_b32_e32 v81, 0xffff0000, v239
	s_add_u32 s98, s14, 0x50000
	s_addc_u32 s99, s15, 0
	global_load_dwordx4 v[236:239], v228, s[98:99] offset:256
	v_pk_fma_f32 v[72:73], v[72:73], v[128:129], v[76:77]
	v_pk_fma_f32 v[70:71], v[70:71], v[126:127], v[74:75]
	v_pk_fma_f32 v[74:75], v[68:69], v[124:125], v[80:81]
	v_pk_fma_f32 v[68:69], v[66:67], v[122:123], v[78:79]
	v_cvt_pk_bf16_f32 v66, v70, v71
	v_cvt_pk_bf16_f32 v67, v72, v73
	s_nop 0
	v_cvt_pk_bf16_f32 v68, v68, v69
	v_cvt_pk_bf16_f32 v69, v74, v75
	s_nop 0
	global_store_dwordx4 v[84:85], v[66:69], off offset:256
	s_waitcnt vmcnt(11)
	s_nop 0
	v_lshlrev_b32_e32 v66, 16, v240
	v_and_b32_e32 v67, 0xffff0000, v240
	v_lshlrev_b32_e32 v68, 16, v241
	v_and_b32_e32 v69, 0xffff0000, v241
	v_lshlrev_b32_e32 v70, 16, v242
	v_and_b32_e32 v71, 0xffff0000, v242
	v_lshlrev_b32_e32 v72, 16, v243
	v_and_b32_e32 v73, 0xffff0000, v243
	s_add_u32 s98, s14, 0x58000
	s_addc_u32 s99, s15, 0
	global_load_dwordx4 v[240:243], v228, s[98:99]
	v_pk_fma_f32 v[64:65], v[64:65], v[136:137], v[68:69]
	v_pk_fma_f32 v[62:63], v[62:63], v[134:135], v[66:67]
	v_pk_fma_f32 v[66:67], v[60:61], v[132:133], v[72:73]
	v_pk_fma_f32 v[60:61], v[58:59], v[130:131], v[70:71]
	v_cvt_pk_bf16_f32 v58, v62, v63
	v_cvt_pk_bf16_f32 v59, v64, v65
	v_lshl_add_u64 v[68:69], s[12:13], 0, v[82:83]
	v_cvt_pk_bf16_f32 v60, v60, v61
	v_cvt_pk_bf16_f32 v61, v66, v67
	v_lshl_add_u64 v[66:67], v[166:167], 0, s[28:29]
	v_lshl_add_u64 v[68:69], v[68:69], 0, v[164:165]
	v_lshl_add_u64 v[70:71], s[14:15], 0, v[66:67]
	global_store_dwordx4 v[68:69], v[58:61], off
	v_lshl_add_u64 v[70:71], v[70:71], 0, v[164:165]
	s_waitcnt vmcnt(11)
	v_lshlrev_b32_e32 v58, 16, v244
	v_and_b32_e32 v59, 0xffff0000, v244
	v_lshlrev_b32_e32 v60, 16, v245
	v_and_b32_e32 v61, 0xffff0000, v245
	v_lshlrev_b32_e32 v62, 16, v246
	v_and_b32_e32 v63, 0xffff0000, v246
	v_lshlrev_b32_e32 v64, 16, v247
	v_and_b32_e32 v65, 0xffff0000, v247
	s_add_u32 s98, s14, 0x58000
	s_addc_u32 s99, s15, 0
	global_load_dwordx4 v[244:247], v228, s[98:99] offset:256
	v_pk_fma_f32 v[52:53], v[52:53], v[128:129], v[60:61]
	v_pk_fma_f32 v[50:51], v[50:51], v[126:127], v[58:59]
	v_pk_fma_f32 v[58:59], v[48:49], v[124:125], v[64:65]
	v_pk_fma_f32 v[48:49], v[46:47], v[122:123], v[62:63]
	v_cvt_pk_bf16_f32 v46, v50, v51
	v_cvt_pk_bf16_f32 v47, v52, v53
	s_nop 0
	v_cvt_pk_bf16_f32 v48, v48, v49
	v_cvt_pk_bf16_f32 v49, v58, v59
	s_nop 0
	global_store_dwordx4 v[68:69], v[46:49], off offset:256
	s_waitcnt vmcnt(11)
; __device__ __forceinline__ u32x4 pack8(const f32x4 a, const f32x4 b) { u32x4 w; w.x = pg8::cvt_pk_bf16(a[0], a[1]); w.y = pg8::cvt_pk_bf16(a[2], a[3]); w.z = pg8::cvt_pk_bf16(b[0], b[1]); w.w = pg8::cvt_pk_bf16(b[2], b[3]); return w; }
;     __device__ __forceinline__ void operator()(const f32x4 (&acc)[2][2][4][2], const pg8::Unit& u, int wr, int wc, int fr_in, int fq_in) const {
;     ...
;         for (int ai = 0; ai < 2; ++ai)
; #pragma unroll
;             for (int m = 0; m < 4; ++m) {
;                 const int row = row0 + ai * 128 + m * 16;
;                 const bf16* bp = xb + (size_t)row * DM + col0;
; #pragma unroll
;                 for (int bj = 0; bj < 2; ++bj) {
;                     const u32x4 bb = *(const u32x4*)(bp + bj * 128);
;                     const f32x4 b0 = (f32x4){bflo(bb.x), bfhi(bb.x), bflo(bb.y), bfhi(bb.y)}, b1 = (f32x4){bflo(bb.z), bfhi(bb.z), bflo(bb.w), bfhi(bb.w)};
;                     *(u32x4*)(out + (size_t)row * DM + col0 + bj * 128) = pack8(b0 + gv[bj][0] * acc[ai][bj][m][0], b1 + gv[bj][1] * acc[ai][bj][m][1]);
;                 }
	s_nop 0
	v_lshlrev_b32_e32 v46, 16, v248
	v_and_b32_e32 v47, 0xffff0000, v248
	v_lshlrev_b32_e32 v48, 16, v249
	v_and_b32_e32 v49, 0xffff0000, v249
	v_lshlrev_b32_e32 v50, 16, v250
	v_and_b32_e32 v51, 0xffff0000, v250
	v_lshlrev_b32_e32 v52, 16, v251
	v_and_b32_e32 v53, 0xffff0000, v251
	v_pk_fma_f32 v[48:49], v[56:57], v[136:137], v[48:49]
	v_pk_fma_f32 v[46:47], v[54:55], v[134:135], v[46:47]
	v_pk_fma_f32 v[52:53], v[44:45], v[132:133], v[52:53]
	v_pk_fma_f32 v[44:45], v[42:43], v[130:131], v[50:51]
	v_cvt_pk_bf16_f32 v42, v46, v47
	v_cvt_pk_bf16_f32 v43, v48, v49
	v_lshl_add_u64 v[50:51], v[166:167], 0, s[30:31]
	v_cvt_pk_bf16_f32 v44, v44, v45
	v_cvt_pk_bf16_f32 v45, v52, v53
	v_lshl_add_u64 v[52:53], s[12:13], 0, v[66:67]
	v_lshl_add_u64 v[52:53], v[52:53], 0, v[164:165]
	v_lshl_add_u64 v[54:55], s[14:15], 0, v[50:51]
	global_store_dwordx4 v[52:53], v[42:45], off
	v_lshl_add_u64 v[54:55], v[54:55], 0, v[164:165]
	s_waitcnt vmcnt(10)
	v_lshlrev_b32_e32 v42, 16, v252
	v_and_b32_e32 v43, 0xffff0000, v252
	v_lshlrev_b32_e32 v44, 16, v253
	v_and_b32_e32 v45, 0xffff0000, v253
	v_lshlrev_b32_e32 v46, 16, v254
	v_and_b32_e32 v47, 0xffff0000, v254
	v_lshlrev_b32_e32 v48, 16, v255
	v_and_b32_e32 v49, 0xffff0000, v255
	v_pk_fma_f32 v[36:37], v[36:37], v[128:129], v[44:45]
	v_pk_fma_f32 v[34:35], v[34:35], v[126:127], v[42:43]
	v_pk_fma_f32 v[42:43], v[32:33], v[124:125], v[48:49]
	v_pk_fma_f32 v[32:33], v[30:31], v[122:123], v[46:47]
	v_cvt_pk_bf16_f32 v30, v34, v35
	v_cvt_pk_bf16_f32 v31, v36, v37
	s_nop 0
	v_cvt_pk_bf16_f32 v32, v32, v33
	v_cvt_pk_bf16_f32 v33, v42, v43
	s_nop 0
	global_store_dwordx4 v[52:53], v[30:33], off offset:256
	s_waitcnt vmcnt(9)
	s_nop 0
	v_lshlrev_b32_e32 v30, 16, v232
	v_and_b32_e32 v31, 0xffff0000, v232
	v_lshlrev_b32_e32 v32, 16, v233
	v_and_b32_e32 v33, 0xffff0000, v233
	v_lshlrev_b32_e32 v34, 16, v234
	v_and_b32_e32 v35, 0xffff0000, v234
	v_lshlrev_b32_e32 v36, 16, v235
	v_and_b32_e32 v37, 0xffff0000, v235
	v_pk_fma_f32 v[32:33], v[40:41], v[136:137], v[32:33]
	v_pk_fma_f32 v[30:31], v[38:39], v[134:135], v[30:31]
	v_pk_fma_f32 v[36:37], v[28:29], v[132:133], v[36:37]
	v_pk_fma_f32 v[28:29], v[26:27], v[130:131], v[34:35]
	v_cvt_pk_bf16_f32 v26, v30, v31
	v_cvt_pk_bf16_f32 v27, v32, v33
	v_lshl_add_u64 v[34:35], v[166:167], 0, s[34:35]
	v_cvt_pk_bf16_f32 v28, v28, v29
	v_cvt_pk_bf16_f32 v29, v36, v37
	v_lshl_add_u64 v[36:37], s[12:13], 0, v[50:51]
	v_lshl_add_u64 v[36:37], v[36:37], 0, v[164:165]
	v_lshl_add_u64 v[38:39], s[14:15], 0, v[34:35]
	global_store_dwordx4 v[36:37], v[26:29], off
	v_lshl_add_u64 v[38:39], v[38:39], 0, v[164:165]
	s_waitcnt vmcnt(8)
	v_lshlrev_b32_e32 v26, 16, v236
	v_and_b32_e32 v27, 0xffff0000, v236
	v_lshlrev_b32_e32 v28, 16, v237
	v_and_b32_e32 v29, 0xffff0000, v237
	v_lshlrev_b32_e32 v30, 16, v238
	v_and_b32_e32 v31, 0xffff0000, v238
	v_lshlrev_b32_e32 v32, 16, v239
	v_and_b32_e32 v33, 0xffff0000, v239
	v_pk_fma_f32 v[20:21], v[20:21], v[128:129], v[28:29]
	v_pk_fma_f32 v[18:19], v[18:19], v[126:127], v[26:27]
	v_pk_fma_f32 v[26:27], v[16:17], v[124:125], v[32:33]
	v_pk_fma_f32 v[16:17], v[14:15], v[122:123], v[30:31]
	v_cvt_pk_bf16_f32 v14, v18, v19
	v_cvt_pk_bf16_f32 v15, v20, v21
	s_nop 0
	v_cvt_pk_bf16_f32 v16, v16, v17
	v_cvt_pk_bf16_f32 v17, v26, v27
	s_nop 0
	global_store_dwordx4 v[36:37], v[14:17], off offset:256
	s_waitcnt vmcnt(7)
	s_nop 0
	v_lshlrev_b32_e32 v14, 16, v240
	v_and_b32_e32 v15, 0xffff0000, v240
	v_lshlrev_b32_e32 v16, 16, v241
	v_and_b32_e32 v17, 0xffff0000, v241
	v_lshlrev_b32_e32 v18, 16, v242
	v_and_b32_e32 v19, 0xffff0000, v242
	v_lshlrev_b32_e32 v20, 16, v243
	v_and_b32_e32 v21, 0xffff0000, v243
	v_pk_fma_f32 v[16:17], v[24:25], v[136:137], v[16:17]
	v_pk_fma_f32 v[14:15], v[22:23], v[134:135], v[14:15]
	v_pk_fma_f32 v[20:21], v[12:13], v[132:133], v[20:21]
	v_pk_fma_f32 v[12:13], v[10:11], v[130:131], v[18:19]
	v_cvt_pk_bf16_f32 v10, v14, v15
	v_cvt_pk_bf16_f32 v11, v16, v17
	v_lshl_add_u64 v[18:19], s[12:13], 0, v[34:35]
	v_cvt_pk_bf16_f32 v12, v12, v13
	v_cvt_pk_bf16_f32 v13, v20, v21
	v_lshl_add_u64 v[18:19], v[18:19], 0, v[164:165]
	global_store_dwordx4 v[18:19], v[10:13], off
	s_waitcnt vmcnt(6)
	s_nop 0
	v_lshlrev_b32_e32 v10, 16, v244
	v_and_b32_e32 v11, 0xffff0000, v244
	v_lshlrev_b32_e32 v12, 16, v245
	v_and_b32_e32 v13, 0xffff0000, v245
	v_lshlrev_b32_e32 v14, 16, v246
	v_and_b32_e32 v15, 0xffff0000, v246
	v_lshlrev_b32_e32 v16, 16, v247
	v_and_b32_e32 v17, 0xffff0000, v247
	v_pk_fma_f32 v[6:7], v[6:7], v[126:127], v[10:11]
	v_pk_fma_f32 v[10:11], v[4:5], v[124:125], v[16:17]
	v_pk_fma_f32 v[4:5], v[2:3], v[122:123], v[14:15]
	v_pk_fma_f32 v[8:9], v[8:9], v[128:129], v[12:13]
	v_cvt_pk_bf16_f32 v2, v6, v7
	s_nop 0
	v_cvt_pk_bf16_f32 v3, v8, v9
	v_cvt_pk_bf16_f32 v4, v4, v5
	v_cvt_pk_bf16_f32 v5, v10, v11
	global_store_dwordx4 v[18:19], v[2:5], off offset:256
	s_cbranch_vccnz .LBB0_1489
	s_andn2_b64 vcc, exec, s[10:11]
	s_cbranch_vccnz .LBB0_1488
	s_barrier
	s_branch .LBB0_1488
